# baseline (speedup 1.0000x reference)
.Lk1_nowarm9:
	buffer_load_dword v8, v1, s[8:11], s40 offen nt
	buffer_load_dword v9, v1, s[8:11], s41 offen nt
	buffer_load_dword v10, v1, s[8:11], s42 offen nt
	buffer_load_dword v11, v1, s[8:11], s43 offen nt
	buffer_load_dword v12, v1, s[8:11], s44 offen nt
	buffer_load_dword v13, v1, s[8:11], s45 offen nt
	buffer_load_dword v14, v1, s[8:11], s46 offen nt
	buffer_load_dword v15, v1, s[8:11], s47 offen nt
	buffer_load_dword v16, v1, s[8:11], s48 offen nt
	buffer_load_dword v17, v1, s[8:11], s49 offen nt
	buffer_load_dword v18, v1, s[8:11], s50 offen nt
	buffer_load_dword v19, v1, s[8:11], s51 offen nt
	buffer_load_dword v20, v1, s[8:11], s52 offen nt
	buffer_load_dword v21, v1, s[8:11], s53 offen nt
	buffer_load_dword v22, v1, s[8:11], s54 offen nt
	buffer_load_dword v23, v1, s[8:11], s55 offen nt
	s_add_u32 s8, s8, 0x4e200
	s_addc_u32 s9, s9, 0
	buffer_load_dword v24, v1, s[8:11], s40 offen nt
	buffer_load_dword v25, v1, s[8:11], s41 offen nt
	buffer_load_dword v26, v1, s[8:11], s42 offen nt
	buffer_load_dword v27, v1, s[8:11], s43 offen nt
	buffer_load_dword v28, v1, s[8:11], s44 offen nt
	buffer_load_dword v29, v1, s[8:11], s45 offen nt
	buffer_load_dword v30, v1, s[8:11], s46 offen nt
	buffer_load_dword v31, v1, s[8:11], s47 offen nt
	buffer_load_dword v32, v1, s[8:11], s48 offen nt
	buffer_load_dword v33, v1, s[8:11], s49 offen nt
	buffer_load_dword v34, v1, s[8:11], s50 offen nt
	buffer_load_dword v35, v1, s[8:11], s51 offen nt
	buffer_load_dword v36, v1, s[8:11], s52 offen nt
	buffer_load_dword v37, v1, s[8:11], s53 offen nt
	buffer_load_dword v38, v1, s[8:11], s54 offen nt
	buffer_load_dword v39, v1, s[8:11], s55 offen nt
	s_add_u32 s8, s8, 0x4e200
	s_addc_u32 s9, s9, 0
	buffer_load_dword v40, v1, s[8:11], s40 offen nt
	buffer_load_dword v41, v1, s[8:11], s41 offen nt
	buffer_load_dword v42, v1, s[8:11], s42 offen nt
	buffer_load_dword v43, v1, s[8:11], s43 offen nt
	buffer_load_dword v44, v1, s[8:11], s44 offen nt
	buffer_load_dword v45, v1, s[8:11], s45 offen nt
	buffer_load_dword v46, v1, s[8:11], s46 offen nt
	buffer_load_dword v47, v1, s[8:11], s47 offen nt
	buffer_load_dword v48, v1, s[8:11], s48 offen nt
	buffer_load_dword v49, v1, s[8:11], s49 offen nt
	buffer_load_dword v50, v1, s[8:11], s50 offen nt
	buffer_load_dword v51, v1, s[8:11], s51 offen nt
	buffer_load_dword v52, v1, s[8:11], s52 offen nt
	buffer_load_dword v53, v1, s[8:11], s53 offen nt
	buffer_load_dword v54, v1, s[8:11], s54 offen nt
	buffer_load_dword v55, v1, s[8:11], s55 offen nt
	s_add_u32 s8, s8, 0x4e200
	s_addc_u32 s9, s9, 0
	buffer_load_dword v56, v1, s[8:11], s40 offen nt
	buffer_load_dword v57, v1, s[8:11], s41 offen nt
	buffer_load_dword v58, v1, s[8:11], s42 offen nt
	buffer_load_dword v59, v1, s[8:11], s43 offen nt
	buffer_load_dword v60, v1, s[8:11], s44 offen nt
	buffer_load_dword v61, v1, s[8:11], s45 offen nt
	buffer_load_dword v62, v1, s[8:11], s46 offen nt
	buffer_load_dword v63, v1, s[8:11], s47 offen nt
	buffer_load_dword v64, v1, s[8:11], s48 offen nt
	buffer_load_dword v65, v1, s[8:11], s49 offen nt
	buffer_load_dword v66, v1, s[8:11], s50 offen nt
	v_mul_u32_u24_e32 v3, 0x147b, v2
	v_lshrrev_b32_e32 v3, 19, v3
	v_mul_u32_u24_e32 v98, 0x64, v3
	v_sub_u32_e32 v98, v2, v98
	v_add_u32_e32 v3, -1, v3
	v_add_u32_e32 v98, -1, v98
	s_movk_i32 s17, 0x62
	v_cmp_gt_u32_e64 s[36:37], 48, v3
	v_cmp_gt_u32_e64 s[38:39], s17, v98
	s_mul_i32 s17, s15, 0x1388
	v_add_lshl_u32 v98, v2, s17, 3
	s_and_b64 s[36:37], s[36:37], s[38:39]
	s_waitcnt vmcnt(55)
	buffer_load_dword v67, v1, s[8:11], s51 offen nt
	buffer_load_dword v68, v1, s[8:11], s52 offen nt
	buffer_load_dword v69, v1, s[8:11], s53 offen nt
	buffer_load_dword v70, v1, s[8:11], s54 offen nt
	buffer_load_dword v71, v1, s[8:11], s55 offen nt
	s_add_u32 s8, s8, 0x4e200
	s_addc_u32 s9, s9, 0
	buffer_load_dword v72, v1, s[8:11], s40 offen nt
	s_waitcnt vmcnt(49)
	v_max3_f32 v76, v8, v9, v10
	v_max3_f32 v76, v76, v11, v12
	v_max3_f32 v76, v76, v13, v14
	v_max3_f32 v76, v76, v15, v16
	v_max3_f32 v76, v76, v17, v18
	v_max3_f32 v76, v76, v19, v20
	v_max3_f32 v76, v76, v21, v22
	v_max_f32_e32 v76, v76, v23
	v_sub_f32_e32 v8, v8, v76
	v_sub_f32_e32 v9, v9, v76
	v_sub_f32_e32 v10, v10, v76
	v_sub_f32_e32 v11, v11, v76
	v_sub_f32_e32 v12, v12, v76
	v_sub_f32_e32 v13, v13, v76
	v_sub_f32_e32 v14, v14, v76
	v_sub_f32_e32 v15, v15, v76
	v_sub_f32_e32 v16, v16, v76
	v_sub_f32_e32 v17, v17, v76
	v_sub_f32_e32 v18, v18, v76
	v_sub_f32_e32 v19, v19, v76
	v_sub_f32_e32 v20, v20, v76
	v_sub_f32_e32 v21, v21, v76
	v_sub_f32_e32 v22, v22, v76
	v_sub_f32_e32 v23, v23, v76
	v_or_b32_e32 v81, 0, v8
	v_or_b32_e32 v82, 1, v9
	v_min_u32_e32 v80, v81, v82
	v_or_b32_e32 v81, 2, v10
	v_or_b32_e32 v82, 3, v11
	v_min3_u32 v80, v80, v81, v82
	v_or_b32_e32 v81, 4, v12
	v_or_b32_e32 v82, 5, v13
	v_min3_u32 v80, v80, v81, v82
	v_or_b32_e32 v81, 6, v14
	v_or_b32_e32 v82, 7, v15
	v_min3_u32 v80, v80, v81, v82
	v_or_b32_e32 v81, 8, v16
	v_or_b32_e32 v82, 9, v17
	v_min3_u32 v80, v80, v81, v82
	v_or_b32_e32 v81, 10, v18
	v_or_b32_e32 v82, 11, v19
	v_min3_u32 v80, v80, v81, v82
	v_or_b32_e32 v81, 12, v20
	v_or_b32_e32 v82, 13, v21
	v_min3_u32 v80, v80, v81, v82
	v_or_b32_e32 v81, 14, v22
	v_or_b32_e32 v82, 15, v23
	v_min3_u32 v80, v80, v81, v82
	v_mul_f32_e32 v8, s14, v8
	v_mul_f32_e32 v9, s14, v9
	v_mul_f32_e32 v10, s14, v10
	v_mul_f32_e32 v11, s14, v11
	v_mul_f32_e32 v12, s14, v12
	v_mul_f32_e32 v13, s14, v13
	v_mul_f32_e32 v14, s14, v14
	v_mul_f32_e32 v15, s14, v15
	v_mul_f32_e32 v16, s14, v16
	v_mul_f32_e32 v17, s14, v17
	v_mul_f32_e32 v18, s14, v18
	v_mul_f32_e32 v19, s14, v19
	v_mul_f32_e32 v20, s14, v20
	v_mul_f32_e32 v21, s14, v21
	v_mul_f32_e32 v22, s14, v22
	v_mul_f32_e32 v23, s14, v23
	v_exp_f32_e32 v8, v8
	v_exp_f32_e32 v9, v9
	v_exp_f32_e32 v10, v10
	v_exp_f32_e32 v11, v11
	v_exp_f32_e32 v12, v12
	v_exp_f32_e32 v13, v13
	v_exp_f32_e32 v14, v14
	v_exp_f32_e32 v15, v15
	v_exp_f32_e32 v16, v16
	v_exp_f32_e32 v17, v17
	v_exp_f32_e32 v18, v18
	v_exp_f32_e32 v19, v19
	v_exp_f32_e32 v20, v20
	v_exp_f32_e32 v21, v21
	v_exp_f32_e32 v22, v22
	v_exp_f32_e32 v23, v23
	v_add_f32_e32 v78, v8, v10
	v_add_f32_e32 v79, v9, v11
	v_add_f32_e32 v78, v78, v12
	v_add_f32_e32 v79, v79, v13
	v_add_f32_e32 v78, v78, v14
	v_add_f32_e32 v79, v79, v15
	v_add_f32_e32 v78, v78, v16
	v_add_f32_e32 v79, v79, v17
	v_add_f32_e32 v78, v78, v18
	v_add_f32_e32 v79, v79, v19
	v_add_f32_e32 v78, v78, v20
	v_add_f32_e32 v79, v79, v21
	v_add_f32_e32 v78, v78, v22
	v_add_f32_e32 v79, v79, v23
	v_add_f32_e32 v78, v78, v79
	v_cvt_f64_f32_e32 v[86:87], v78
	v_mov_b32_e32 v75, v80
	v_mov_b32_e32 v73, v76
	s_waitcnt vmcnt(33)
	v_max3_f32 v76, v24, v25, v26
	v_max3_f32 v76, v76, v27, v28
	v_max3_f32 v76, v76, v29, v30
	v_max3_f32 v76, v76, v31, v32
	v_max3_f32 v76, v76, v33, v34
	v_max3_f32 v76, v76, v35, v36
	v_max3_f32 v76, v76, v37, v38
	v_max_f32_e32 v76, v76, v39
	v_max_f32_e32 v77, v73, v76
	v_cmp_gt_f32_e64 s[26:27], v76, v73
	v_sub_f32_e32 v83, v73, v77
	v_mul_f32_e32 v83, s14, v83
	v_exp_f32_e32 v83, v83
	v_sub_f32_e32 v24, v24, v77
	v_sub_f32_e32 v25, v25, v77
	v_sub_f32_e32 v26, v26, v77
	v_sub_f32_e32 v27, v27, v77
	v_sub_f32_e32 v28, v28, v77
	v_sub_f32_e32 v29, v29, v77
	v_sub_f32_e32 v30, v30, v77
	v_sub_f32_e32 v31, v31, v77
	v_sub_f32_e32 v32, v32, v77
	v_sub_f32_e32 v33, v33, v77
	v_sub_f32_e32 v34, v34, v77
	v_sub_f32_e32 v35, v35, v77
	v_sub_f32_e32 v36, v36, v77
	v_sub_f32_e32 v37, v37, v77
	v_sub_f32_e32 v38, v38, v77
	v_sub_f32_e32 v39, v39, v77
	v_cvt_f64_f32_e32 v[84:85], v83
	v_or_b32_e32 v81, 16, v24
	v_or_b32_e32 v82, 17, v25
	v_min_u32_e32 v80, v81, v82
	v_or_b32_e32 v81, 18, v26
	v_or_b32_e32 v82, 19, v27
	v_min3_u32 v80, v80, v81, v82
	v_or_b32_e32 v81, 20, v28
	v_or_b32_e32 v82, 21, v29
	v_min3_u32 v80, v80, v81, v82
	v_or_b32_e32 v81, 22, v30
	v_or_b32_e32 v82, 23, v31
	v_min3_u32 v80, v80, v81, v82
	v_or_b32_e32 v81, 24, v32
	v_or_b32_e32 v82, 25, v33
	v_min3_u32 v80, v80, v81, v82
	v_or_b32_e32 v81, 26, v34
	v_or_b32_e32 v82, 27, v35
	v_min3_u32 v80, v80, v81, v82
	v_or_b32_e32 v81, 28, v36
	v_or_b32_e32 v82, 29, v37
	v_min3_u32 v80, v80, v81, v82
	v_or_b32_e32 v81, 30, v38
	v_or_b32_e32 v82, 31, v39
	v_min3_u32 v80, v80, v81, v82
	v_mul_f64 v[86:87], v[86:87], v[84:85]
	v_mul_f32_e32 v24, s14, v24
	v_mul_f32_e32 v25, s14, v25
	v_mul_f32_e32 v26, s14, v26
	v_mul_f32_e32 v27, s14, v27
	v_mul_f32_e32 v28, s14, v28
	v_mul_f32_e32 v29, s14, v29
	v_mul_f32_e32 v30, s14, v30
	v_mul_f32_e32 v31, s14, v31
	v_mul_f32_e32 v32, s14, v32
	v_mul_f32_e32 v33, s14, v33
	v_mul_f32_e32 v34, s14, v34
	v_mul_f32_e32 v35, s14, v35
	v_mul_f32_e32 v36, s14, v36
	v_mul_f32_e32 v37, s14, v37
	v_mul_f32_e32 v38, s14, v38
	v_mul_f32_e32 v39, s14, v39
	v_exp_f32_e32 v24, v24
	v_exp_f32_e32 v25, v25
	v_exp_f32_e32 v26, v26
	v_exp_f32_e32 v27, v27
	v_exp_f32_e32 v28, v28
	v_exp_f32_e32 v29, v29
	v_exp_f32_e32 v30, v30
	v_exp_f32_e32 v31, v31
	v_exp_f32_e32 v32, v32
	v_exp_f32_e32 v33, v33
	v_exp_f32_e32 v34, v34
	v_exp_f32_e32 v35, v35
	v_exp_f32_e32 v36, v36
	v_exp_f32_e32 v37, v37
	v_exp_f32_e32 v38, v38
	v_exp_f32_e32 v39, v39
	v_add_f32_e32 v78, v24, v26
	v_add_f32_e32 v79, v25, v27
	v_add_f32_e32 v78, v78, v28
	v_add_f32_e32 v79, v79, v29
	v_add_f32_e32 v78, v78, v30
	v_add_f32_e32 v79, v79, v31
	v_add_f32_e32 v78, v78, v32
	v_add_f32_e32 v79, v79, v33
	v_add_f32_e32 v78, v78, v34
	v_add_f32_e32 v79, v79, v35
	v_add_f32_e32 v78, v78, v36
	v_add_f32_e32 v79, v79, v37
	v_add_f32_e32 v78, v78, v38
	v_add_f32_e32 v79, v79, v39
	v_add_f32_e32 v78, v78, v79
	v_cvt_f64_f32_e32 v[84:85], v78
	v_cndmask_b32_e64 v75, v75, v80, s[26:27]
	v_mov_b32_e32 v73, v77
	v_add_f64 v[86:87], v[86:87], v[84:85]
	s_waitcnt vmcnt(17)
	v_max3_f32 v76, v40, v41, v42
	v_max3_f32 v76, v76, v43, v44
	v_max3_f32 v76, v76, v45, v46
	v_max3_f32 v76, v76, v47, v48
	v_max3_f32 v76, v76, v49, v50
	v_max3_f32 v76, v76, v51, v52
	v_max3_f32 v76, v76, v53, v54
	v_max_f32_e32 v76, v76, v55
	v_max_f32_e32 v77, v73, v76
	v_cmp_gt_f32_e64 s[26:27], v76, v73
	v_sub_f32_e32 v83, v73, v77
	v_mul_f32_e32 v83, s14, v83
	v_exp_f32_e32 v83, v83
	v_sub_f32_e32 v40, v40, v77
	v_sub_f32_e32 v41, v41, v77
	v_sub_f32_e32 v42, v42, v77
	v_sub_f32_e32 v43, v43, v77
	v_sub_f32_e32 v44, v44, v77
	v_sub_f32_e32 v45, v45, v77
	v_sub_f32_e32 v46, v46, v77
	v_sub_f32_e32 v47, v47, v77
	v_sub_f32_e32 v48, v48, v77
	v_sub_f32_e32 v49, v49, v77
	v_sub_f32_e32 v50, v50, v77
	v_sub_f32_e32 v51, v51, v77
	v_sub_f32_e32 v52, v52, v77
	v_sub_f32_e32 v53, v53, v77
	v_sub_f32_e32 v54, v54, v77
	v_sub_f32_e32 v55, v55, v77
	v_cvt_f64_f32_e32 v[84:85], v83
	v_or_b32_e32 v81, 32, v40
	v_or_b32_e32 v82, 33, v41
	v_min_u32_e32 v80, v81, v82
	v_or_b32_e32 v81, 34, v42
	v_or_b32_e32 v82, 35, v43
	v_min3_u32 v80, v80, v81, v82
	v_or_b32_e32 v81, 36, v44
	v_or_b32_e32 v82, 37, v45
	v_min3_u32 v80, v80, v81, v82
	v_or_b32_e32 v81, 38, v46
	v_or_b32_e32 v82, 39, v47
	v_min3_u32 v80, v80, v81, v82
	v_or_b32_e32 v81, 40, v48
	v_or_b32_e32 v82, 41, v49
	v_min3_u32 v80, v80, v81, v82
	v_or_b32_e32 v81, 42, v50
	v_or_b32_e32 v82, 43, v51
	v_min3_u32 v80, v80, v81, v82
	v_or_b32_e32 v81, 44, v52
	v_or_b32_e32 v82, 45, v53
	v_min3_u32 v80, v80, v81, v82
	v_or_b32_e32 v81, 46, v54
	v_or_b32_e32 v82, 47, v55
	v_min3_u32 v80, v80, v81, v82
	v_mul_f64 v[86:87], v[86:87], v[84:85]
	v_mul_f32_e32 v40, s14, v40
	v_mul_f32_e32 v41, s14, v41
	v_mul_f32_e32 v42, s14, v42
	v_mul_f32_e32 v43, s14, v43
	v_mul_f32_e32 v44, s14, v44
	v_mul_f32_e32 v45, s14, v45
	v_mul_f32_e32 v46, s14, v46
	v_mul_f32_e32 v47, s14, v47
	v_mul_f32_e32 v48, s14, v48
	v_mul_f32_e32 v49, s14, v49
	v_mul_f32_e32 v50, s14, v50
	v_mul_f32_e32 v51, s14, v51
	v_mul_f32_e32 v52, s14, v52
	v_mul_f32_e32 v53, s14, v53
	v_mul_f32_e32 v54, s14, v54
	v_mul_f32_e32 v55, s14, v55
	v_exp_f32_e32 v40, v40
	v_exp_f32_e32 v41, v41
	v_exp_f32_e32 v42, v42
	v_exp_f32_e32 v43, v43
	v_exp_f32_e32 v44, v44
	v_exp_f32_e32 v45, v45
	v_exp_f32_e32 v46, v46
	v_exp_f32_e32 v47, v47
	v_exp_f32_e32 v48, v48
	v_exp_f32_e32 v49, v49
	v_exp_f32_e32 v50, v50
	v_exp_f32_e32 v51, v51
	v_exp_f32_e32 v52, v52
	v_exp_f32_e32 v53, v53
	v_exp_f32_e32 v54, v54
	v_exp_f32_e32 v55, v55
	v_add_f32_e32 v78, v40, v42
	v_add_f32_e32 v79, v41, v43
	v_add_f32_e32 v78, v78, v44
	v_add_f32_e32 v79, v79, v45
	v_add_f32_e32 v78, v78, v46
	v_add_f32_e32 v79, v79, v47
	v_add_f32_e32 v78, v78, v48
	v_add_f32_e32 v79, v79, v49
	v_add_f32_e32 v78, v78, v50
	v_add_f32_e32 v79, v79, v51
	v_add_f32_e32 v78, v78, v52
	v_add_f32_e32 v79, v79, v53
	v_add_f32_e32 v78, v78, v54
	v_add_f32_e32 v79, v79, v55
	v_add_f32_e32 v78, v78, v79
	v_cvt_f64_f32_e32 v[84:85], v78
	v_cndmask_b32_e64 v75, v75, v80, s[26:27]
	v_mov_b32_e32 v73, v77
	v_add_f64 v[86:87], v[86:87], v[84:85]
	s_waitcnt vmcnt(9)
	v_max3_f32 v76, v56, v57, v58
	v_max3_f32 v76, v76, v59, v60
	v_max3_f32 v76, v76, v61, v62
	v_max_f32_e32 v76, v76, v63
	v_max_f32_e32 v77, v73, v76
	v_cmp_gt_f32_e64 s[26:27], v76, v73
	v_sub_f32_e32 v83, v73, v77
	v_mul_f32_e32 v83, s14, v83
	v_exp_f32_e32 v83, v83
	v_sub_f32_e32 v56, v56, v77
	v_sub_f32_e32 v57, v57, v77
	v_sub_f32_e32 v58, v58, v77
	v_sub_f32_e32 v59, v59, v77
	v_sub_f32_e32 v60, v60, v77
	v_sub_f32_e32 v61, v61, v77
	v_sub_f32_e32 v62, v62, v77
	v_sub_f32_e32 v63, v63, v77
	v_cvt_f64_f32_e32 v[84:85], v83
	v_or_b32_e32 v81, 48, v56
	v_or_b32_e32 v82, 49, v57
	v_min_u32_e32 v80, v81, v82
	v_or_b32_e32 v81, 50, v58
	v_or_b32_e32 v82, 51, v59
	v_min3_u32 v80, v80, v81, v82
	v_or_b32_e32 v81, 52, v60
	v_or_b32_e32 v82, 53, v61
	v_min3_u32 v80, v80, v81, v82
	v_or_b32_e32 v81, 54, v62
	v_or_b32_e32 v82, 55, v63
	v_min3_u32 v80, v80, v81, v82
	v_mul_f64 v[86:87], v[86:87], v[84:85]
	v_mul_f32_e32 v56, s14, v56
	v_mul_f32_e32 v57, s14, v57
	v_mul_f32_e32 v58, s14, v58
	v_mul_f32_e32 v59, s14, v59
	v_mul_f32_e32 v60, s14, v60
	v_mul_f32_e32 v61, s14, v61
	v_mul_f32_e32 v62, s14, v62
	v_mul_f32_e32 v63, s14, v63
	v_exp_f32_e32 v56, v56
	v_exp_f32_e32 v57, v57
	v_exp_f32_e32 v58, v58
	v_exp_f32_e32 v59, v59
	v_exp_f32_e32 v60, v60
	v_exp_f32_e32 v61, v61
	v_exp_f32_e32 v62, v62
	v_exp_f32_e32 v63, v63
	v_add_f32_e32 v78, v56, v58
	v_add_f32_e32 v79, v57, v59
	v_add_f32_e32 v78, v78, v60
	v_add_f32_e32 v79, v79, v61
	v_add_f32_e32 v78, v78, v62
	v_add_f32_e32 v79, v79, v63
	v_add_f32_e32 v78, v78, v79
	v_cvt_f64_f32_e32 v[84:85], v78
	v_cndmask_b32_e64 v75, v75, v80, s[26:27]
	v_mov_b32_e32 v73, v77
	v_add_f64 v[86:87], v[86:87], v[84:85]
	s_waitcnt vmcnt(5)
	v_max3_f32 v76, v64, v65, v66
	v_max_f32_e32 v76, v76, v67
	v_max_f32_e32 v77, v73, v76
	v_cmp_gt_f32_e64 s[26:27], v76, v73
	v_sub_f32_e32 v83, v73, v77
	v_mul_f32_e32 v83, s14, v83
	v_exp_f32_e32 v83, v83
	v_sub_f32_e32 v64, v64, v77
	v_sub_f32_e32 v65, v65, v77
	v_sub_f32_e32 v66, v66, v77
	v_sub_f32_e32 v67, v67, v77
	v_cvt_f64_f32_e32 v[84:85], v83
	v_or_b32_e32 v81, 56, v64
	v_or_b32_e32 v82, 57, v65
	v_min_u32_e32 v80, v81, v82
	v_or_b32_e32 v81, 58, v66
	v_or_b32_e32 v82, 59, v67
	v_min3_u32 v80, v80, v81, v82
	v_mul_f64 v[86:87], v[86:87], v[84:85]
	v_mul_f32_e32 v64, s14, v64
	v_mul_f32_e32 v65, s14, v65
	v_mul_f32_e32 v66, s14, v66
	v_mul_f32_e32 v67, s14, v67
	v_exp_f32_e32 v64, v64
	v_exp_f32_e32 v65, v65
	v_exp_f32_e32 v66, v66
	v_exp_f32_e32 v67, v67
	v_add_f32_e32 v78, v64, v66
	v_add_f32_e32 v79, v65, v67
	v_add_f32_e32 v78, v78, v79
	v_cvt_f64_f32_e32 v[84:85], v78
	v_cndmask_b32_e64 v75, v75, v80, s[26:27]
	v_mov_b32_e32 v73, v77
	v_add_f64 v[86:87], v[86:87], v[84:85]
	s_waitcnt vmcnt(4)
	v_max_f32_e32 v77, v73, v68
	v_cmp_gt_f32_e64 s[26:27], v68, v73
	v_sub_f32_e32 v83, v73, v77
	v_sub_f32_e32 v68, v68, v77
	v_mul_f32_e32 v83, s14, v83
	v_mul_f32_e32 v68, s14, v68
	v_exp_f32_e32 v83, v83
	v_exp_f32_e32 v68, v68
	v_cndmask_b32_e64 v75, v75, 60, s[26:27]
	v_cvt_f64_f32_e32 v[84:85], v83
	v_cvt_f64_f32_e32 v[90:91], v68
	v_mul_f64 v[86:87], v[86:87], v[84:85]
	v_mov_b32_e32 v73, v77
	v_add_f64 v[86:87], v[86:87], v[90:91]
	s_waitcnt vmcnt(3)
	v_max_f32_e32 v77, v73, v69
	v_cmp_gt_f32_e64 s[26:27], v69, v73
	v_sub_f32_e32 v83, v73, v77
	v_sub_f32_e32 v69, v69, v77
	v_mul_f32_e32 v83, s14, v83
	v_mul_f32_e32 v69, s14, v69
	v_exp_f32_e32 v83, v83
	v_exp_f32_e32 v69, v69
	v_cndmask_b32_e64 v75, v75, 61, s[26:27]
	v_cvt_f64_f32_e32 v[84:85], v83
	v_cvt_f64_f32_e32 v[90:91], v69
	v_mul_f64 v[86:87], v[86:87], v[84:85]
	v_mov_b32_e32 v73, v77
	v_add_f64 v[86:87], v[86:87], v[90:91]
	s_waitcnt vmcnt(2)
	v_max_f32_e32 v77, v73, v70
	v_cmp_gt_f32_e64 s[26:27], v70, v73
	v_sub_f32_e32 v83, v73, v77
	v_sub_f32_e32 v70, v70, v77
	v_mul_f32_e32 v83, s14, v83
	v_mul_f32_e32 v70, s14, v70
	v_exp_f32_e32 v83, v83
	v_exp_f32_e32 v70, v70
	v_cndmask_b32_e64 v75, v75, 62, s[26:27]
	v_cvt_f64_f32_e32 v[84:85], v83
	v_cvt_f64_f32_e32 v[90:91], v70
	v_mul_f64 v[86:87], v[86:87], v[84:85]
	v_mov_b32_e32 v73, v77
	v_add_f64 v[86:87], v[86:87], v[90:91]
	s_waitcnt vmcnt(1)
	v_max_f32_e32 v77, v73, v71
	v_cmp_gt_f32_e64 s[26:27], v71, v73
	v_sub_f32_e32 v83, v73, v77
	v_sub_f32_e32 v71, v71, v77
	v_mul_f32_e32 v83, s14, v83
	v_mul_f32_e32 v71, s14, v71
	v_exp_f32_e32 v83, v83
	v_exp_f32_e32 v71, v71
	v_cndmask_b32_e64 v75, v75, 63, s[26:27]
	v_cvt_f64_f32_e32 v[84:85], v83
	v_cvt_f64_f32_e32 v[90:91], v71
	v_mul_f64 v[86:87], v[86:87], v[84:85]
	v_mov_b32_e32 v73, v77
	v_add_f64 v[86:87], v[86:87], v[90:91]
	s_waitcnt vmcnt(0)
	v_max_f32_e32 v77, v73, v72
	v_cmp_gt_f32_e64 s[26:27], v72, v73
	v_sub_f32_e32 v83, v73, v77
	v_sub_f32_e32 v72, v72, v77
	v_mul_f32_e32 v83, s14, v83
	v_mul_f32_e32 v72, s14, v72
	v_exp_f32_e32 v83, v83
	v_exp_f32_e32 v72, v72
	v_cndmask_b32_e64 v75, v75, 64, s[26:27]
	v_cvt_f64_f32_e32 v[84:85], v83
	v_cvt_f64_f32_e32 v[90:91], v72
	v_mul_f64 v[86:87], v[86:87], v[84:85]
	v_add_f64 v[86:87], v[86:87], v[90:91]
	v_rcp_f64_e32 v[88:89], v[86:87]
	v_cmp_gt_u32_e32 vcc, 64, v75
	s_and_b64 vcc, vcc, s[36:37]
	v_fma_f64 v[90:91], -v[86:87], v[88:89], 1.0
	v_fma_f64 v[88:89], v[90:91], v[88:89], v[88:89]
	v_cvt_f32_f64_e32 v3, v[88:89]
	v_cndmask_b32_e32 v74, 0, v3, vcc
	global_store_dwordx2 v98, v[74:75], s[6:7]
